# dynamic 8-row chunk assignment across waves (LDS cursor), two 8-row buffers, register fp64 accumulation over sorted rows
# speedup vs baseline: 1.0388x; 1.0388x over previous
_Z7vq_mainPKfPKiS0_PfPhPdPi:
	s_load_dwordx4 s[4:7], s[0:1], 0x0
	s_load_dwordx2 s[22:23], s[0:1], 0x10
	s_load_dwordx2 s[20:21], s[0:1], 0x18
	s_load_dwordx4 s[12:15], s[0:1], 0x20
	s_load_dwordx2 s[10:11], s[0:1], 0x30
	s_and_b32 s3, s2, 7
	s_lshl_b32 s3, s3, 6
	s_lshr_b32 s16, s2, 3
	s_add_i32 s16, s16, s3
	s_lshr_b32 s18, s16, 5
	s_mov_b32 s19, 0
	s_and_b32 s28, s16, 31
	s_lshl_b32 s28, s28, 4
	s_add_i32 s29, s28, 1
	v_readfirstlane_b32 s17, v0
	v_and_b32_e32 v1, 63, v0
	v_lshlrev_b32_e32 v66, 4, v0
	s_lshr_b32 s17, s17, 6
	s_lshl_b32 s24, s17, 4
	s_lshl_b32 s30, s18, 15
	s_lshl_b32 s31, s18, 23
	v_add_u32_e32 v67, 0x1000, v66
	v_add_u32_e32 v68, 0x2000, v66
	v_add_u32_e32 v69, 0x3000, v66
	v_add_u32_e32 v70, 0x4000, v66
	v_add_u32_e32 v71, 0x5000, v66
	v_add_u32_e32 v72, 0x6000, v66
	v_add_u32_e32 v73, 0x7000, v66
	s_waitcnt lgkmcnt(0)
	s_add_u32 s34, s6, s30
	s_addc_u32 s35, s7, 0
	s_add_u32 s32, s4, s31
	s_addc_u32 s33, s5, 0
	global_load_dwordx4 v[74:77], v66, s[34:35]
	global_load_dwordx4 v[78:81], v67, s[34:35]
	global_load_dwordx4 v[82:85], v68, s[34:35]
	global_load_dwordx4 v[86:89], v69, s[34:35]
	global_load_dwordx4 v[90:93], v70, s[34:35]
	global_load_dwordx4 v[94:97], v71, s[34:35]
	global_load_dwordx4 v[98:101], v72, s[34:35]
	global_load_dwordx4 v[102:105], v73, s[34:35]
	v_and_b32_e32 v150, 15, v0
	v_or_b32_e32 v150, s24, v150
	v_and_b32_e32 v151, 48, v0
	v_lshl_or_b32 v150, v150, 10, v151
	global_load_dwordx4 v[62:65], v150, s[22:23] offset:0
	global_load_dwordx4 v[58:61], v150, s[22:23] offset:64
	global_load_dwordx4 v[54:57], v150, s[22:23] offset:128
	global_load_dwordx4 v[50:53], v150, s[22:23] offset:192
	global_load_dwordx4 v[46:49], v150, s[22:23] offset:256
	global_load_dwordx4 v[42:45], v150, s[22:23] offset:320
	global_load_dwordx4 v[38:41], v150, s[22:23] offset:384
	global_load_dwordx4 v[34:37], v150, s[22:23] offset:448
	global_load_dwordx4 v[30:33], v150, s[22:23] offset:512
	global_load_dwordx4 v[26:29], v150, s[22:23] offset:576
	global_load_dwordx4 v[22:25], v150, s[22:23] offset:640
	global_load_dwordx4 v[18:21], v150, s[22:23] offset:704
	global_load_dwordx4 v[14:17], v150, s[22:23] offset:768
	global_load_dwordx4 v[10:13], v150, s[22:23] offset:832
	global_load_dwordx4 v[6:9], v150, s[22:23] offset:896
	global_load_dwordx4 v[2:5], v150, s[22:23] offset:960
	v_mov_b32_e32 v142, 1
	v_mov_b32_e32 v143, 4
	v_mov_b32_e32 v144, 0x11100
	v_lshlrev_b32_e32 v145, 8, v0
	v_lshlrev_b32_e32 v148, 3, v0
	v_mov_b32_e32 v152, 0
	v_mov_b32_e32 v153, 0
	ds_write_b64 v148, v[152:153] offset:32768
	ds_write_b64 v148, v[152:153] offset:34832
	ds_write_b64 v148, v[152:153] offset:36896
	ds_write_b64 v148, v[152:153] offset:38960
	ds_write_b64 v148, v[152:153] offset:41024
	ds_write_b64 v148, v[152:153] offset:43088
	ds_write_b64 v148, v[152:153] offset:45152
	ds_write_b64 v148, v[152:153] offset:47216
	ds_write_b64 v148, v[152:153] offset:49280
	ds_write_b64 v148, v[152:153] offset:51344
	ds_write_b64 v148, v[152:153] offset:53408
	ds_write_b64 v148, v[152:153] offset:55472
	ds_write_b64 v148, v[152:153] offset:57536
	ds_write_b64 v148, v[152:153] offset:59600
	ds_write_b64 v148, v[152:153] offset:61664
	ds_write_b64 v148, v[152:153] offset:63728
	v_cmp_gt_u32_e32 vcc, 16, v0
	s_and_saveexec_b64 s[30:31], vcc
	v_lshl_add_u32 v151, v0, 2, v144
	ds_write_b32 v151, v152
	v_mov_b32_e32 v150, 0x11540
	ds_write_b32 v150, v152
	s_mov_b64 exec, s[30:31]
	s_waitcnt lgkmcnt(0)
	s_barrier
	s_waitcnt vmcnt(16)
	v_subrev_u32_e32 v74, s29, v74
	v_subrev_u32_e32 v75, s29, v75
	v_subrev_u32_e32 v76, s29, v76
	v_subrev_u32_e32 v77, s29, v77
	v_subrev_u32_e32 v78, s29, v78
	v_subrev_u32_e32 v79, s29, v79
	v_subrev_u32_e32 v80, s29, v80
	v_subrev_u32_e32 v81, s29, v81
	v_subrev_u32_e32 v82, s29, v82
	v_subrev_u32_e32 v83, s29, v83
	v_subrev_u32_e32 v84, s29, v84
	v_subrev_u32_e32 v85, s29, v85
	v_subrev_u32_e32 v86, s29, v86
	v_subrev_u32_e32 v87, s29, v87
	v_subrev_u32_e32 v88, s29, v88
	v_subrev_u32_e32 v89, s29, v89
	v_subrev_u32_e32 v90, s29, v90
	v_subrev_u32_e32 v91, s29, v91
	v_subrev_u32_e32 v92, s29, v92
	v_subrev_u32_e32 v93, s29, v93
	v_subrev_u32_e32 v94, s29, v94
	v_subrev_u32_e32 v95, s29, v95
	v_subrev_u32_e32 v96, s29, v96
	v_subrev_u32_e32 v97, s29, v97
	v_subrev_u32_e32 v98, s29, v98
	v_subrev_u32_e32 v99, s29, v99
	v_subrev_u32_e32 v100, s29, v100
	v_subrev_u32_e32 v101, s29, v101
	v_subrev_u32_e32 v102, s29, v102
	v_subrev_u32_e32 v103, s29, v103
	v_subrev_u32_e32 v104, s29, v104
	v_subrev_u32_e32 v105, s29, v105
	v_cmp_gt_u32_e64 s[36:37], 16, v74
	v_cmp_gt_u32_e64 s[38:39], 16, v75
	v_cmp_gt_u32_e64 s[40:41], 16, v76
	v_cmp_gt_u32_e64 s[42:43], 16, v77
	v_cmp_gt_u32_e64 s[44:45], 16, v78
	v_cmp_gt_u32_e64 s[46:47], 16, v79
	v_cmp_gt_u32_e64 s[48:49], 16, v80
	v_cmp_gt_u32_e64 s[50:51], 16, v81
	v_cmp_gt_u32_e64 s[52:53], 16, v82
	v_cmp_gt_u32_e64 s[54:55], 16, v83
	v_cmp_gt_u32_e64 s[56:57], 16, v84
	v_cmp_gt_u32_e64 s[58:59], 16, v85
	v_cmp_gt_u32_e64 s[60:61], 16, v86
	v_cmp_gt_u32_e64 s[62:63], 16, v87
	v_cmp_gt_u32_e64 s[64:65], 16, v88
	v_cmp_gt_u32_e64 s[66:67], 16, v89
	v_cmp_gt_u32_e64 s[68:69], 16, v90
	v_cmp_gt_u32_e64 s[70:71], 16, v91
	v_cmp_gt_u32_e64 s[72:73], 16, v92
	v_cmp_gt_u32_e64 s[74:75], 16, v93
	v_cmp_gt_u32_e64 s[76:77], 16, v94
	v_cmp_gt_u32_e64 s[78:79], 16, v95
	v_cmp_gt_u32_e64 s[80:81], 16, v96
	v_cmp_gt_u32_e64 s[82:83], 16, v97
	v_cmp_gt_u32_e64 s[84:85], 16, v98
	v_cmp_gt_u32_e64 s[86:87], 16, v99
	v_cmp_gt_u32_e64 s[88:89], 16, v100
	v_cmp_gt_u32_e64 s[90:91], 16, v101
	v_cmp_gt_u32_e64 s[92:93], 16, v102
	v_cmp_gt_u32_e64 s[94:95], 16, v103
	v_cmp_gt_u32_e64 s[96:97], 16, v104
	v_cmp_gt_u32_e64 s[98:99], 16, v105
	s_mov_b64 exec, s[36:37]
	v_lshl_add_u32 v74, v74, 2, v144
	ds_add_u32 v74, v142
	s_mov_b64 exec, s[38:39]
	v_lshl_add_u32 v75, v75, 2, v144
	ds_add_u32 v75, v142
	s_mov_b64 exec, s[40:41]
	v_lshl_add_u32 v76, v76, 2, v144
	ds_add_u32 v76, v142
	s_mov_b64 exec, s[42:43]
	v_lshl_add_u32 v77, v77, 2, v144
	ds_add_u32 v77, v142
	s_mov_b64 exec, s[44:45]
	v_lshl_add_u32 v78, v78, 2, v144
	ds_add_u32 v78, v142
	s_mov_b64 exec, s[46:47]
	v_lshl_add_u32 v79, v79, 2, v144
	ds_add_u32 v79, v142
	s_mov_b64 exec, s[48:49]
	v_lshl_add_u32 v80, v80, 2, v144
	ds_add_u32 v80, v142
	s_mov_b64 exec, s[50:51]
	v_lshl_add_u32 v81, v81, 2, v144
	ds_add_u32 v81, v142
	s_mov_b64 exec, s[52:53]
	v_lshl_add_u32 v82, v82, 2, v144
	ds_add_u32 v82, v142
	s_mov_b64 exec, s[54:55]
	v_lshl_add_u32 v83, v83, 2, v144
	ds_add_u32 v83, v142
	s_mov_b64 exec, s[56:57]
	v_lshl_add_u32 v84, v84, 2, v144
	ds_add_u32 v84, v142
	s_mov_b64 exec, s[58:59]
	v_lshl_add_u32 v85, v85, 2, v144
	ds_add_u32 v85, v142
	s_mov_b64 exec, s[60:61]
	v_lshl_add_u32 v86, v86, 2, v144
	ds_add_u32 v86, v142
	s_mov_b64 exec, s[62:63]
	v_lshl_add_u32 v87, v87, 2, v144
	ds_add_u32 v87, v142
	s_mov_b64 exec, s[64:65]
	v_lshl_add_u32 v88, v88, 2, v144
	ds_add_u32 v88, v142
	s_mov_b64 exec, s[66:67]
	v_lshl_add_u32 v89, v89, 2, v144
	ds_add_u32 v89, v142
	s_mov_b64 exec, s[68:69]
	v_lshl_add_u32 v90, v90, 2, v144
	ds_add_u32 v90, v142
	s_mov_b64 exec, s[70:71]
	v_lshl_add_u32 v91, v91, 2, v144
	ds_add_u32 v91, v142
	s_mov_b64 exec, s[72:73]
	v_lshl_add_u32 v92, v92, 2, v144
	ds_add_u32 v92, v142
	s_mov_b64 exec, s[74:75]
	v_lshl_add_u32 v93, v93, 2, v144
	ds_add_u32 v93, v142
	s_mov_b64 exec, s[76:77]
	v_lshl_add_u32 v94, v94, 2, v144
	ds_add_u32 v94, v142
	s_mov_b64 exec, s[78:79]
	v_lshl_add_u32 v95, v95, 2, v144
	ds_add_u32 v95, v142
	s_mov_b64 exec, s[80:81]
	v_lshl_add_u32 v96, v96, 2, v144
	ds_add_u32 v96, v142
	s_mov_b64 exec, s[82:83]
	v_lshl_add_u32 v97, v97, 2, v144
	ds_add_u32 v97, v142
	s_mov_b64 exec, s[84:85]
	v_lshl_add_u32 v98, v98, 2, v144
	ds_add_u32 v98, v142
	s_mov_b64 exec, s[86:87]
	v_lshl_add_u32 v99, v99, 2, v144
	ds_add_u32 v99, v142
	s_mov_b64 exec, s[88:89]
	v_lshl_add_u32 v100, v100, 2, v144
	ds_add_u32 v100, v142
	s_mov_b64 exec, s[90:91]
	v_lshl_add_u32 v101, v101, 2, v144
	ds_add_u32 v101, v142
	s_mov_b64 exec, s[92:93]
	v_lshl_add_u32 v102, v102, 2, v144
	ds_add_u32 v102, v142
	s_mov_b64 exec, s[94:95]
	v_lshl_add_u32 v103, v103, 2, v144
	ds_add_u32 v103, v142
	s_mov_b64 exec, s[96:97]
	v_lshl_add_u32 v104, v104, 2, v144
	ds_add_u32 v104, v142
	s_mov_b64 exec, s[98:99]
	v_lshl_add_u32 v105, v105, 2, v144
	ds_add_u32 v105, v142
	s_mov_b64 exec, -1
	s_waitcnt lgkmcnt(0)
	s_barrier
	v_and_b32_e32 v67, 15, v0
	v_lshl_add_u32 v67, v67, 2, v144
	ds_read_b32 v68, v67
	s_waitcnt lgkmcnt(0)
	v_mov_b32_e32 v69, v68
	s_nop 1
	v_add_u32_dpp v69, v69, v69 row_shr:1 row_mask:0xf bank_mask:0xf bound_ctrl:1
	s_nop 1
	v_add_u32_dpp v69, v69, v69 row_shr:2 row_mask:0xf bank_mask:0xf bound_ctrl:1
	s_nop 1
	v_add_u32_dpp v69, v69, v69 row_shr:4 row_mask:0xf bank_mask:0xf bound_ctrl:1
	s_nop 1
	v_add_u32_dpp v69, v69, v69 row_shr:8 row_mask:0xf bank_mask:0xf bound_ctrl:1
	s_nop 1
	v_sub_u32_e32 v70, v69, v68
	v_lshlrev_b32_e32 v70, 2, v70
	v_readlane_b32 s8, v69, 15
	s_cmp_lg_u32 s17, 0
	s_cbranch_scc1 .Lfront_nocursor
	v_cmp_gt_u32_e32 vcc, 16, v1
	s_and_saveexec_b64 s[30:31], vcc
	ds_write_b32 v67, v70 offset:64
	s_mov_b64 exec, s[30:31]
.Lfront_nocursor:
	s_waitcnt lgkmcnt(0)
	s_barrier
	s_mov_b64 exec, s[36:37]
	ds_add_rtn_u32 v106, v74, v143 offset:64
	s_mov_b64 exec, s[38:39]
	ds_add_rtn_u32 v107, v75, v143 offset:64
	s_mov_b64 exec, s[40:41]
	ds_add_rtn_u32 v108, v76, v143 offset:64
	s_mov_b64 exec, s[42:43]
	ds_add_rtn_u32 v109, v77, v143 offset:64
	s_mov_b64 exec, s[44:45]
	ds_add_rtn_u32 v110, v78, v143 offset:64
	s_mov_b64 exec, s[46:47]
	ds_add_rtn_u32 v111, v79, v143 offset:64
	s_mov_b64 exec, s[48:49]
	ds_add_rtn_u32 v112, v80, v143 offset:64
	s_mov_b64 exec, s[50:51]
	ds_add_rtn_u32 v113, v81, v143 offset:64
	s_mov_b64 exec, s[52:53]
	ds_add_rtn_u32 v114, v82, v143 offset:64
	s_mov_b64 exec, s[54:55]
	ds_add_rtn_u32 v115, v83, v143 offset:64
	s_mov_b64 exec, s[56:57]
	ds_add_rtn_u32 v116, v84, v143 offset:64
	s_mov_b64 exec, s[58:59]
	ds_add_rtn_u32 v117, v85, v143 offset:64
	s_mov_b64 exec, s[60:61]
	ds_add_rtn_u32 v118, v86, v143 offset:64
	s_mov_b64 exec, s[62:63]
	ds_add_rtn_u32 v119, v87, v143 offset:64
	s_mov_b64 exec, s[64:65]
	ds_add_rtn_u32 v120, v88, v143 offset:64
	s_mov_b64 exec, s[66:67]
	ds_add_rtn_u32 v121, v89, v143 offset:64
	s_mov_b64 exec, s[68:69]
	ds_add_rtn_u32 v122, v90, v143 offset:64
	s_mov_b64 exec, s[70:71]
	ds_add_rtn_u32 v123, v91, v143 offset:64
	s_mov_b64 exec, s[72:73]
	ds_add_rtn_u32 v124, v92, v143 offset:64
	s_mov_b64 exec, s[74:75]
	ds_add_rtn_u32 v125, v93, v143 offset:64
	s_mov_b64 exec, s[76:77]
	ds_add_rtn_u32 v126, v94, v143 offset:64
	s_mov_b64 exec, s[78:79]
	ds_add_rtn_u32 v127, v95, v143 offset:64
	s_mov_b64 exec, s[80:81]
	ds_add_rtn_u32 v128, v96, v143 offset:64
	s_mov_b64 exec, s[82:83]
	ds_add_rtn_u32 v129, v97, v143 offset:64
	s_mov_b64 exec, s[84:85]
	ds_add_rtn_u32 v130, v98, v143 offset:64
	s_mov_b64 exec, s[86:87]
	ds_add_rtn_u32 v131, v99, v143 offset:64
	s_mov_b64 exec, s[88:89]
	ds_add_rtn_u32 v132, v100, v143 offset:64
	s_mov_b64 exec, s[90:91]
	ds_add_rtn_u32 v133, v101, v143 offset:64
	s_mov_b64 exec, s[92:93]
	ds_add_rtn_u32 v134, v102, v143 offset:64
	s_mov_b64 exec, s[94:95]
	ds_add_rtn_u32 v135, v103, v143 offset:64
	s_mov_b64 exec, s[96:97]
	ds_add_rtn_u32 v136, v104, v143 offset:64
	s_mov_b64 exec, s[98:99]
	ds_add_rtn_u32 v137, v105, v143 offset:64
	s_mov_b64 exec, -1
	v_add_u32_e32 v146, 0x0, v145
	v_and_or_b32 v146, v74, 60, v146
	s_waitcnt lgkmcnt(0)
	s_mov_b64 exec, s[36:37]
	ds_write_b32 v106, v146
	s_mov_b64 exec, -1
	v_add_u32_e32 v147, 0x40, v145
	v_and_or_b32 v147, v75, 60, v147
	s_mov_b64 exec, s[38:39]
	ds_write_b32 v107, v147
	s_mov_b64 exec, -1
	v_add_u32_e32 v146, 0x80, v145
	v_and_or_b32 v146, v76, 60, v146
	s_mov_b64 exec, s[40:41]
	ds_write_b32 v108, v146
	s_mov_b64 exec, -1
	v_add_u32_e32 v147, 0xc0, v145
	v_and_or_b32 v147, v77, 60, v147
	s_mov_b64 exec, s[42:43]
	ds_write_b32 v109, v147
	s_mov_b64 exec, -1
	v_add_u32_e32 v146, 0x10000, v145
	v_and_or_b32 v146, v78, 60, v146
	s_mov_b64 exec, s[44:45]
	ds_write_b32 v110, v146
	s_mov_b64 exec, -1
	v_add_u32_e32 v147, 0x10040, v145
	v_and_or_b32 v147, v79, 60, v147
	s_mov_b64 exec, s[46:47]
	ds_write_b32 v111, v147
	s_mov_b64 exec, -1
	v_add_u32_e32 v146, 0x10080, v145
	v_and_or_b32 v146, v80, 60, v146
	s_mov_b64 exec, s[48:49]
	ds_write_b32 v112, v146
	s_mov_b64 exec, -1
	v_add_u32_e32 v147, 0x100c0, v145
	v_and_or_b32 v147, v81, 60, v147
	s_mov_b64 exec, s[50:51]
	ds_write_b32 v113, v147
	s_mov_b64 exec, -1
	v_add_u32_e32 v146, 0x20000, v145
	v_and_or_b32 v146, v82, 60, v146
	s_mov_b64 exec, s[52:53]
	ds_write_b32 v114, v146
	s_mov_b64 exec, -1
	v_add_u32_e32 v147, 0x20040, v145
	v_and_or_b32 v147, v83, 60, v147
	s_mov_b64 exec, s[54:55]
	ds_write_b32 v115, v147
	s_mov_b64 exec, -1
	v_add_u32_e32 v146, 0x20080, v145
	v_and_or_b32 v146, v84, 60, v146
	s_mov_b64 exec, s[56:57]
	ds_write_b32 v116, v146
	s_mov_b64 exec, -1
	v_add_u32_e32 v147, 0x200c0, v145
	v_and_or_b32 v147, v85, 60, v147
	s_mov_b64 exec, s[58:59]
	ds_write_b32 v117, v147
	s_mov_b64 exec, -1
	v_add_u32_e32 v146, 0x30000, v145
	v_and_or_b32 v146, v86, 60, v146
	s_mov_b64 exec, s[60:61]
	ds_write_b32 v118, v146
	s_mov_b64 exec, -1
	v_add_u32_e32 v147, 0x30040, v145
	v_and_or_b32 v147, v87, 60, v147
	s_mov_b64 exec, s[62:63]
	ds_write_b32 v119, v147
	s_mov_b64 exec, -1
	v_add_u32_e32 v146, 0x30080, v145
	v_and_or_b32 v146, v88, 60, v146
	s_mov_b64 exec, s[64:65]
	ds_write_b32 v120, v146
	s_mov_b64 exec, -1
	v_add_u32_e32 v147, 0x300c0, v145
	v_and_or_b32 v147, v89, 60, v147
	s_mov_b64 exec, s[66:67]
	ds_write_b32 v121, v147
	s_mov_b64 exec, -1
	v_add_u32_e32 v146, 0x40000, v145
	v_and_or_b32 v146, v90, 60, v146
	s_mov_b64 exec, s[68:69]
	ds_write_b32 v122, v146
	s_mov_b64 exec, -1
	v_add_u32_e32 v147, 0x40040, v145
	v_and_or_b32 v147, v91, 60, v147
	s_mov_b64 exec, s[70:71]
	ds_write_b32 v123, v147
	s_mov_b64 exec, -1
	v_add_u32_e32 v146, 0x40080, v145
	v_and_or_b32 v146, v92, 60, v146
	s_mov_b64 exec, s[72:73]
	ds_write_b32 v124, v146
	s_mov_b64 exec, -1
	v_add_u32_e32 v147, 0x400c0, v145
	v_and_or_b32 v147, v93, 60, v147
	s_mov_b64 exec, s[74:75]
	ds_write_b32 v125, v147
	s_mov_b64 exec, -1
	v_add_u32_e32 v146, 0x50000, v145
	v_and_or_b32 v146, v94, 60, v146
	s_mov_b64 exec, s[76:77]
	ds_write_b32 v126, v146
	s_mov_b64 exec, -1
	v_add_u32_e32 v147, 0x50040, v145
	v_and_or_b32 v147, v95, 60, v147
	s_mov_b64 exec, s[78:79]
	ds_write_b32 v127, v147
	s_mov_b64 exec, -1
	v_add_u32_e32 v146, 0x50080, v145
	v_and_or_b32 v146, v96, 60, v146
	s_mov_b64 exec, s[80:81]
	ds_write_b32 v128, v146
	s_mov_b64 exec, -1
	v_add_u32_e32 v147, 0x500c0, v145
	v_and_or_b32 v147, v97, 60, v147
	s_mov_b64 exec, s[82:83]
	ds_write_b32 v129, v147
	s_mov_b64 exec, -1
	v_add_u32_e32 v146, 0x60000, v145
	v_and_or_b32 v146, v98, 60, v146
	s_mov_b64 exec, s[84:85]
	ds_write_b32 v130, v146
	s_mov_b64 exec, -1
	v_add_u32_e32 v147, 0x60040, v145
	v_and_or_b32 v147, v99, 60, v147
	s_mov_b64 exec, s[86:87]
	ds_write_b32 v131, v147
	s_mov_b64 exec, -1
	v_add_u32_e32 v146, 0x60080, v145
	v_and_or_b32 v146, v100, 60, v146
	s_mov_b64 exec, s[88:89]
	ds_write_b32 v132, v146
	s_mov_b64 exec, -1
	v_add_u32_e32 v147, 0x600c0, v145
	v_and_or_b32 v147, v101, 60, v147
	s_mov_b64 exec, s[90:91]
	ds_write_b32 v133, v147
	s_mov_b64 exec, -1
	v_add_u32_e32 v146, 0x70000, v145
	v_and_or_b32 v146, v102, 60, v146
	s_mov_b64 exec, s[92:93]
	ds_write_b32 v134, v146
	s_mov_b64 exec, -1
	v_add_u32_e32 v147, 0x70040, v145
	v_and_or_b32 v147, v103, 60, v147
	s_mov_b64 exec, s[94:95]
	ds_write_b32 v135, v147
	s_mov_b64 exec, -1
	v_add_u32_e32 v146, 0x70080, v145
	v_and_or_b32 v146, v104, 60, v146
	s_mov_b64 exec, s[96:97]
	ds_write_b32 v136, v146
	s_mov_b64 exec, -1
	v_add_u32_e32 v147, 0x700c0, v145
	v_and_or_b32 v147, v105, 60, v147
	s_mov_b64 exec, s[98:99]
	ds_write_b32 v137, v147
	s_mov_b64 exec, -1
	s_waitcnt lgkmcnt(0)
	s_barrier
	s_add_i32 s53, s8, 7
	s_lshr_b32 s53, s53, 3
	v_lshlrev_b32_e32 v218, 4, v1
	v_lshlrev_b32_e32 v219, 3, v1
	v_mov_b32_e32 v223, 0x11540
	v_and_b32_e32 v221, 7, v1
	v_mov_b32_e32 v200, 0
	v_mov_b32_e32 v201, 0
	v_mov_b32_e32 v202, 0
	v_mov_b32_e32 v203, 0
	v_mov_b32_e32 v204, 0
	v_mov_b32_e32 v205, 0
	v_mov_b32_e32 v206, 0
	v_mov_b32_e32 v207, 0
	s_mov_b32 s50, -1
	s_mov_b64 exec, 1
	ds_add_rtn_u32 v222, v223, v142
	s_mov_b64 exec, -1
	s_waitcnt lgkmcnt(0)
	v_readfirstlane_b32 s54, v222
	s_mov_b64 exec, 1
	ds_add_rtn_u32 v222, v223, v142
	s_mov_b64 exec, -1
	s_waitcnt lgkmcnt(0)
	v_readfirstlane_b32 s55, v222
	s_cmp_ge_u32 s54, s53
	s_cbranch_scc1 .Lg_alldone
	s_lshl_b32 s46, s54, 3
	v_add_u32_e32 v220, s46, v221
	v_cmp_gt_u32_e32 vcc, s8, v220
	v_lshlrev_b32_e32 v220, 2, v220
	ds_read_b32 v216, v220
	s_waitcnt lgkmcnt(0)
	v_cndmask_b32_e32 v216, 1, v216, vcc
	s_nop 1
	v_readlane_b32 s50, v216, 0
	s_bfe_u32 s50, s50, 0x40002
	v_readlane_b32 s40, v216, 0
	s_bfe_u32 s60, s40, 0x40002
	s_bitcmp1_b32 s40, 0
	s_cselect_b32 s60, 16, s60
	s_and_b32 s40, s40, 0xffffffc0
	s_lshl_b32 s40, s40, 4
	s_add_u32 s42, s32, s40
	s_addc_u32 s43, s33, 0
	global_load_dwordx4 v[66:69], v218, s[42:43] nt
	v_readlane_b32 s40, v216, 1
	s_bfe_u32 s61, s40, 0x40002
	s_bitcmp1_b32 s40, 0
	s_cselect_b32 s61, 16, s61
	s_and_b32 s40, s40, 0xffffffc0
	s_lshl_b32 s40, s40, 4
	s_add_u32 s42, s32, s40
	s_addc_u32 s43, s33, 0
	global_load_dwordx4 v[70:73], v218, s[42:43] nt
	v_readlane_b32 s40, v216, 2
	s_bfe_u32 s62, s40, 0x40002
	s_bitcmp1_b32 s40, 0
	s_cselect_b32 s62, 16, s62
	s_and_b32 s40, s40, 0xffffffc0
	s_lshl_b32 s40, s40, 4
	s_add_u32 s42, s32, s40
	s_addc_u32 s43, s33, 0
	global_load_dwordx4 v[74:77], v218, s[42:43] nt
	v_readlane_b32 s40, v216, 3
	s_bfe_u32 s63, s40, 0x40002
	s_bitcmp1_b32 s40, 0
	s_cselect_b32 s63, 16, s63
	s_and_b32 s40, s40, 0xffffffc0
	s_lshl_b32 s40, s40, 4
	s_add_u32 s42, s32, s40
	s_addc_u32 s43, s33, 0
	global_load_dwordx4 v[78:81], v218, s[42:43] nt
	v_readlane_b32 s40, v216, 4
	s_bfe_u32 s64, s40, 0x40002
	s_bitcmp1_b32 s40, 0
	s_cselect_b32 s64, 16, s64
	s_and_b32 s40, s40, 0xffffffc0
	s_lshl_b32 s40, s40, 4
	s_add_u32 s42, s32, s40
	s_addc_u32 s43, s33, 0
	global_load_dwordx4 v[82:85], v218, s[42:43] nt
	v_readlane_b32 s40, v216, 5
	s_bfe_u32 s65, s40, 0x40002
	s_bitcmp1_b32 s40, 0
	s_cselect_b32 s65, 16, s65
	s_and_b32 s40, s40, 0xffffffc0
	s_lshl_b32 s40, s40, 4
	s_add_u32 s42, s32, s40
	s_addc_u32 s43, s33, 0
	global_load_dwordx4 v[86:89], v218, s[42:43] nt
	v_readlane_b32 s40, v216, 6
	s_bfe_u32 s66, s40, 0x40002
	s_bitcmp1_b32 s40, 0
	s_cselect_b32 s66, 16, s66
	s_and_b32 s40, s40, 0xffffffc0
	s_lshl_b32 s40, s40, 4
	s_add_u32 s42, s32, s40
	s_addc_u32 s43, s33, 0
	global_load_dwordx4 v[90:93], v218, s[42:43] nt
	v_readlane_b32 s40, v216, 7
	s_bfe_u32 s67, s40, 0x40002
	s_bitcmp1_b32 s40, 0
	s_cselect_b32 s67, 16, s67
	s_and_b32 s40, s40, 0xffffffc0
	s_lshl_b32 s40, s40, 4
	s_add_u32 s42, s32, s40
	s_addc_u32 s43, s33, 0
	global_load_dwordx4 v[94:97], v218, s[42:43] nt
	s_cmp_ge_u32 s55, s53
	s_cbranch_scc1 .Lg_drainA
	s_lshl_b32 s46, s55, 3
	v_add_u32_e32 v220, s46, v221
	v_cmp_gt_u32_e32 vcc, s8, v220
	v_lshlrev_b32_e32 v220, 2, v220
	ds_read_b32 v217, v220
	s_waitcnt lgkmcnt(0)
	v_cndmask_b32_e32 v217, 1, v217, vcc
	s_nop 1
	v_readlane_b32 s40, v217, 0
	s_bfe_u32 s68, s40, 0x40002
	s_bitcmp1_b32 s40, 0
	s_cselect_b32 s68, 16, s68
	s_and_b32 s40, s40, 0xffffffc0
	s_lshl_b32 s40, s40, 4
	s_add_u32 s42, s32, s40
	s_addc_u32 s43, s33, 0
	global_load_dwordx4 v[98:101], v218, s[42:43] nt
	v_readlane_b32 s40, v217, 1
	s_bfe_u32 s69, s40, 0x40002
	s_bitcmp1_b32 s40, 0
	s_cselect_b32 s69, 16, s69
	s_and_b32 s40, s40, 0xffffffc0
	s_lshl_b32 s40, s40, 4
	s_add_u32 s42, s32, s40
	s_addc_u32 s43, s33, 0
	global_load_dwordx4 v[102:105], v218, s[42:43] nt
	v_readlane_b32 s40, v217, 2
	s_bfe_u32 s70, s40, 0x40002
	s_bitcmp1_b32 s40, 0
	s_cselect_b32 s70, 16, s70
	s_and_b32 s40, s40, 0xffffffc0
	s_lshl_b32 s40, s40, 4
	s_add_u32 s42, s32, s40
	s_addc_u32 s43, s33, 0
	global_load_dwordx4 v[106:109], v218, s[42:43] nt
	v_readlane_b32 s40, v217, 3
	s_bfe_u32 s71, s40, 0x40002
	s_bitcmp1_b32 s40, 0
	s_cselect_b32 s71, 16, s71
	s_and_b32 s40, s40, 0xffffffc0
	s_lshl_b32 s40, s40, 4
	s_add_u32 s42, s32, s40
	s_addc_u32 s43, s33, 0
	global_load_dwordx4 v[110:113], v218, s[42:43] nt
	v_readlane_b32 s40, v217, 4
	s_bfe_u32 s72, s40, 0x40002
	s_bitcmp1_b32 s40, 0
	s_cselect_b32 s72, 16, s72
	s_and_b32 s40, s40, 0xffffffc0
	s_lshl_b32 s40, s40, 4
	s_add_u32 s42, s32, s40
	s_addc_u32 s43, s33, 0
	global_load_dwordx4 v[114:117], v218, s[42:43] nt
	v_readlane_b32 s40, v217, 5
	s_bfe_u32 s73, s40, 0x40002
	s_bitcmp1_b32 s40, 0
	s_cselect_b32 s73, 16, s73
	s_and_b32 s40, s40, 0xffffffc0
	s_lshl_b32 s40, s40, 4
	s_add_u32 s42, s32, s40
	s_addc_u32 s43, s33, 0
	global_load_dwordx4 v[118:121], v218, s[42:43] nt
	v_readlane_b32 s40, v217, 6
	s_bfe_u32 s74, s40, 0x40002
	s_bitcmp1_b32 s40, 0
	s_cselect_b32 s74, 16, s74
	s_and_b32 s40, s40, 0xffffffc0
	s_lshl_b32 s40, s40, 4
	s_add_u32 s42, s32, s40
	s_addc_u32 s43, s33, 0
	global_load_dwordx4 v[122:125], v218, s[42:43] nt
	v_readlane_b32 s40, v217, 7
	s_bfe_u32 s75, s40, 0x40002
	s_bitcmp1_b32 s40, 0
	s_cselect_b32 s75, 16, s75
	s_and_b32 s40, s40, 0xffffffc0
	s_lshl_b32 s40, s40, 4
	s_add_u32 s42, s32, s40
	s_addc_u32 s43, s33, 0
	global_load_dwordx4 v[126:129], v218, s[42:43] nt
.Lg_loop:
	s_mov_b64 exec, 1
	ds_add_rtn_u32 v222, v223, v142
	s_mov_b64 exec, -1
	s_waitcnt vmcnt(15)
	s_cmp_eq_u32 s60, 16
	s_cbranch_scc1 .Lc_A8_skip0
	s_cmp_lg_u32 s60, s50
	s_cbranch_scc1 .Lc_A8_flush0

.Lc_A8_skip0:
	s_waitcnt vmcnt(14)
	s_cmp_eq_u32 s61, 16
	s_cbranch_scc1 .Lc_A8_skip1
	s_cmp_lg_u32 s61, s50
	s_cbranch_scc1 .Lc_A8_flush1

.Lc_A8_skip1:
	s_waitcnt vmcnt(13)
	s_cmp_eq_u32 s62, 16
	s_cbranch_scc1 .Lc_A8_skip2
	s_cmp_lg_u32 s62, s50
	s_cbranch_scc1 .Lc_A8_flush2

.Lc_A8_skip2:
	s_waitcnt vmcnt(12)
	s_cmp_eq_u32 s63, 16
	s_cbranch_scc1 .Lc_A8_skip3
	s_cmp_lg_u32 s63, s50
	s_cbranch_scc1 .Lc_A8_flush3

.Lc_A8_skip3:
	s_waitcnt vmcnt(11)
	s_cmp_eq_u32 s64, 16
	s_cbranch_scc1 .Lc_A8_skip4
	s_cmp_lg_u32 s64, s50
	s_cbranch_scc1 .Lc_A8_flush4

.Lc_A8_skip4:
	s_waitcnt vmcnt(10)
	s_cmp_eq_u32 s65, 16
	s_cbranch_scc1 .Lc_A8_skip5
	s_cmp_lg_u32 s65, s50
	s_cbranch_scc1 .Lc_A8_flush5

.Lc_A8_skip5:
	s_waitcnt vmcnt(9)
	s_cmp_eq_u32 s66, 16
	s_cbranch_scc1 .Lc_A8_skip6
	s_cmp_lg_u32 s66, s50
	s_cbranch_scc1 .Lc_A8_flush6

.Lc_A8_skip6:
	s_waitcnt vmcnt(8)
	s_cmp_eq_u32 s67, 16
	s_cbranch_scc1 .Lc_A8_skip7
	s_cmp_lg_u32 s67, s50
	s_cbranch_scc1 .Lc_A8_flush7

.Lc_A8_skip7:
	s_waitcnt lgkmcnt(0)
	v_readfirstlane_b32 s54, v222
	s_cmp_ge_u32 s54, s53
	s_cbranch_scc1 .Lg_drainB
	s_lshl_b32 s46, s54, 3
	v_add_u32_e32 v220, s46, v221
	v_cmp_gt_u32_e32 vcc, s8, v220
	v_lshlrev_b32_e32 v220, 2, v220
	ds_read_b32 v216, v220
	s_waitcnt lgkmcnt(0)
	v_cndmask_b32_e32 v216, 1, v216, vcc
	s_nop 1
	v_readlane_b32 s40, v216, 0
	s_bfe_u32 s60, s40, 0x40002
	s_bitcmp1_b32 s40, 0
	s_cselect_b32 s60, 16, s60
	s_and_b32 s40, s40, 0xffffffc0
	s_lshl_b32 s40, s40, 4
	s_add_u32 s42, s32, s40
	s_addc_u32 s43, s33, 0
	global_load_dwordx4 v[66:69], v218, s[42:43] nt
	v_readlane_b32 s40, v216, 1
	s_bfe_u32 s61, s40, 0x40002
	s_bitcmp1_b32 s40, 0
	s_cselect_b32 s61, 16, s61
	s_and_b32 s40, s40, 0xffffffc0
	s_lshl_b32 s40, s40, 4
	s_add_u32 s42, s32, s40
	s_addc_u32 s43, s33, 0
	global_load_dwordx4 v[70:73], v218, s[42:43] nt
	v_readlane_b32 s40, v216, 2
	s_bfe_u32 s62, s40, 0x40002
	s_bitcmp1_b32 s40, 0
	s_cselect_b32 s62, 16, s62
	s_and_b32 s40, s40, 0xffffffc0
	s_lshl_b32 s40, s40, 4
	s_add_u32 s42, s32, s40
	s_addc_u32 s43, s33, 0
	global_load_dwordx4 v[74:77], v218, s[42:43] nt
	v_readlane_b32 s40, v216, 3
	s_bfe_u32 s63, s40, 0x40002
	s_bitcmp1_b32 s40, 0
	s_cselect_b32 s63, 16, s63
	s_and_b32 s40, s40, 0xffffffc0
	s_lshl_b32 s40, s40, 4
	s_add_u32 s42, s32, s40
	s_addc_u32 s43, s33, 0
	global_load_dwordx4 v[78:81], v218, s[42:43] nt
	v_readlane_b32 s40, v216, 4
	s_bfe_u32 s64, s40, 0x40002
	s_bitcmp1_b32 s40, 0
	s_cselect_b32 s64, 16, s64
	s_and_b32 s40, s40, 0xffffffc0
	s_lshl_b32 s40, s40, 4
	s_add_u32 s42, s32, s40
	s_addc_u32 s43, s33, 0
	global_load_dwordx4 v[82:85], v218, s[42:43] nt
	v_readlane_b32 s40, v216, 5
	s_bfe_u32 s65, s40, 0x40002
	s_bitcmp1_b32 s40, 0
	s_cselect_b32 s65, 16, s65
	s_and_b32 s40, s40, 0xffffffc0
	s_lshl_b32 s40, s40, 4
	s_add_u32 s42, s32, s40
	s_addc_u32 s43, s33, 0
	global_load_dwordx4 v[86:89], v218, s[42:43] nt
	v_readlane_b32 s40, v216, 6
	s_bfe_u32 s66, s40, 0x40002
	s_bitcmp1_b32 s40, 0
	s_cselect_b32 s66, 16, s66
	s_and_b32 s40, s40, 0xffffffc0
	s_lshl_b32 s40, s40, 4
	s_add_u32 s42, s32, s40
	s_addc_u32 s43, s33, 0
	global_load_dwordx4 v[90:93], v218, s[42:43] nt
	v_readlane_b32 s40, v216, 7
	s_bfe_u32 s67, s40, 0x40002
	s_bitcmp1_b32 s40, 0
	s_cselect_b32 s67, 16, s67
	s_and_b32 s40, s40, 0xffffffc0
	s_lshl_b32 s40, s40, 4
	s_add_u32 s42, s32, s40
	s_addc_u32 s43, s33, 0
	global_load_dwordx4 v[94:97], v218, s[42:43] nt
	s_mov_b64 exec, 1
	ds_add_rtn_u32 v222, v223, v142
	s_mov_b64 exec, -1
	s_waitcnt vmcnt(15)
	s_cmp_eq_u32 s68, 16
	s_cbranch_scc1 .Lc_B8_skip8
	s_cmp_lg_u32 s68, s50
	s_cbranch_scc1 .Lc_B8_flush8

.Lc_B8_skip8:
	s_waitcnt vmcnt(14)
	s_cmp_eq_u32 s69, 16
	s_cbranch_scc1 .Lc_B8_skip9
	s_cmp_lg_u32 s69, s50
	s_cbranch_scc1 .Lc_B8_flush9

.Lc_B8_skip9:
	s_waitcnt vmcnt(13)
	s_cmp_eq_u32 s70, 16
	s_cbranch_scc1 .Lc_B8_skip10
	s_cmp_lg_u32 s70, s50
	s_cbranch_scc1 .Lc_B8_flush10

.Lc_B8_skip10:
	s_waitcnt vmcnt(12)
	s_cmp_eq_u32 s71, 16
	s_cbranch_scc1 .Lc_B8_skip11
	s_cmp_lg_u32 s71, s50
	s_cbranch_scc1 .Lc_B8_flush11

.Lc_B8_skip11:
	s_waitcnt vmcnt(11)
	s_cmp_eq_u32 s72, 16
	s_cbranch_scc1 .Lc_B8_skip12
	s_cmp_lg_u32 s72, s50
	s_cbranch_scc1 .Lc_B8_flush12

.Lc_B8_skip12:
	s_waitcnt vmcnt(10)
	s_cmp_eq_u32 s73, 16
	s_cbranch_scc1 .Lc_B8_skip13
	s_cmp_lg_u32 s73, s50
	s_cbranch_scc1 .Lc_B8_flush13

.Lc_B8_skip13:
	s_waitcnt vmcnt(9)
	s_cmp_eq_u32 s74, 16
	s_cbranch_scc1 .Lc_B8_skip14
	s_cmp_lg_u32 s74, s50
	s_cbranch_scc1 .Lc_B8_flush14

.Lc_B8_skip14:
	s_waitcnt vmcnt(8)
	s_cmp_eq_u32 s75, 16
	s_cbranch_scc1 .Lc_B8_skip15
	s_cmp_lg_u32 s75, s50
	s_cbranch_scc1 .Lc_B8_flush15

.Lc_B8_skip15:
	s_waitcnt lgkmcnt(0)
	v_readfirstlane_b32 s55, v222
	s_cmp_ge_u32 s55, s53
	s_cbranch_scc1 .Lg_drainA
	s_lshl_b32 s46, s55, 3
	v_add_u32_e32 v220, s46, v221
	v_cmp_gt_u32_e32 vcc, s8, v220
	v_lshlrev_b32_e32 v220, 2, v220
	ds_read_b32 v217, v220
	s_waitcnt lgkmcnt(0)
	v_cndmask_b32_e32 v217, 1, v217, vcc
	s_nop 1
	v_readlane_b32 s40, v217, 0
	s_bfe_u32 s68, s40, 0x40002
	s_bitcmp1_b32 s40, 0
	s_cselect_b32 s68, 16, s68
	s_and_b32 s40, s40, 0xffffffc0
	s_lshl_b32 s40, s40, 4
	s_add_u32 s42, s32, s40
	s_addc_u32 s43, s33, 0
	global_load_dwordx4 v[98:101], v218, s[42:43] nt
	v_readlane_b32 s40, v217, 1
	s_bfe_u32 s69, s40, 0x40002
	s_bitcmp1_b32 s40, 0
	s_cselect_b32 s69, 16, s69
	s_and_b32 s40, s40, 0xffffffc0
	s_lshl_b32 s40, s40, 4
	s_add_u32 s42, s32, s40
	s_addc_u32 s43, s33, 0
	global_load_dwordx4 v[102:105], v218, s[42:43] nt
	v_readlane_b32 s40, v217, 2
	s_bfe_u32 s70, s40, 0x40002
	s_bitcmp1_b32 s40, 0
	s_cselect_b32 s70, 16, s70
	s_and_b32 s40, s40, 0xffffffc0
	s_lshl_b32 s40, s40, 4
	s_add_u32 s42, s32, s40
	s_addc_u32 s43, s33, 0
	global_load_dwordx4 v[106:109], v218, s[42:43] nt
	v_readlane_b32 s40, v217, 3
	s_bfe_u32 s71, s40, 0x40002
	s_bitcmp1_b32 s40, 0
	s_cselect_b32 s71, 16, s71
	s_and_b32 s40, s40, 0xffffffc0
	s_lshl_b32 s40, s40, 4
	s_add_u32 s42, s32, s40
	s_addc_u32 s43, s33, 0
	global_load_dwordx4 v[110:113], v218, s[42:43] nt
	v_readlane_b32 s40, v217, 4
	s_bfe_u32 s72, s40, 0x40002
	s_bitcmp1_b32 s40, 0
	s_cselect_b32 s72, 16, s72
	s_and_b32 s40, s40, 0xffffffc0
	s_lshl_b32 s40, s40, 4
	s_add_u32 s42, s32, s40
	s_addc_u32 s43, s33, 0
	global_load_dwordx4 v[114:117], v218, s[42:43] nt
	v_readlane_b32 s40, v217, 5
	s_bfe_u32 s73, s40, 0x40002
	s_bitcmp1_b32 s40, 0
	s_cselect_b32 s73, 16, s73
	s_and_b32 s40, s40, 0xffffffc0
	s_lshl_b32 s40, s40, 4
	s_add_u32 s42, s32, s40
	s_addc_u32 s43, s33, 0
	global_load_dwordx4 v[118:121], v218, s[42:43] nt
	v_readlane_b32 s40, v217, 6
	s_bfe_u32 s74, s40, 0x40002
	s_bitcmp1_b32 s40, 0
	s_cselect_b32 s74, 16, s74
	s_and_b32 s40, s40, 0xffffffc0
	s_lshl_b32 s40, s40, 4
	s_add_u32 s42, s32, s40
	s_addc_u32 s43, s33, 0
	global_load_dwordx4 v[122:125], v218, s[42:43] nt
	v_readlane_b32 s40, v217, 7
	s_bfe_u32 s75, s40, 0x40002
	s_bitcmp1_b32 s40, 0
	s_cselect_b32 s75, 16, s75
	s_and_b32 s40, s40, 0xffffffc0
	s_lshl_b32 s40, s40, 4
	s_add_u32 s42, s32, s40
	s_addc_u32 s43, s33, 0
	global_load_dwordx4 v[126:129], v218, s[42:43] nt
	s_branch .Lg_loop
.Lg_drainA:
	s_waitcnt vmcnt(7)
	s_cmp_eq_u32 s60, 16
	s_cbranch_scc1 .Lc_A0_skip0
	s_cmp_lg_u32 s60, s50
	s_cbranch_scc1 .Lc_A0_flush0

.Lc_A0_skip0:
	s_waitcnt vmcnt(6)
	s_cmp_eq_u32 s61, 16
	s_cbranch_scc1 .Lc_A0_skip1
	s_cmp_lg_u32 s61, s50
	s_cbranch_scc1 .Lc_A0_flush1

.Lc_A0_skip1:
	s_waitcnt vmcnt(5)
	s_cmp_eq_u32 s62, 16
	s_cbranch_scc1 .Lc_A0_skip2
	s_cmp_lg_u32 s62, s50
	s_cbranch_scc1 .Lc_A0_flush2

.Lc_A0_skip2:
	s_waitcnt vmcnt(4)
	s_cmp_eq_u32 s63, 16
	s_cbranch_scc1 .Lc_A0_skip3
	s_cmp_lg_u32 s63, s50
	s_cbranch_scc1 .Lc_A0_flush3

.Lc_A0_skip3:
	s_waitcnt vmcnt(3)
	s_cmp_eq_u32 s64, 16
	s_cbranch_scc1 .Lc_A0_skip4
	s_cmp_lg_u32 s64, s50
	s_cbranch_scc1 .Lc_A0_flush4

.Lc_A0_skip4:
	s_waitcnt vmcnt(2)
	s_cmp_eq_u32 s65, 16
	s_cbranch_scc1 .Lc_A0_skip5
	s_cmp_lg_u32 s65, s50
	s_cbranch_scc1 .Lc_A0_flush5

.Lc_A0_skip5:
	s_waitcnt vmcnt(1)
	s_cmp_eq_u32 s66, 16
	s_cbranch_scc1 .Lc_A0_skip6
	s_cmp_lg_u32 s66, s50
	s_cbranch_scc1 .Lc_A0_flush6

.Lc_A0_skip6:
	s_waitcnt vmcnt(0)
	s_cmp_eq_u32 s67, 16
	s_cbranch_scc1 .Lc_A0_skip7
	s_cmp_lg_u32 s67, s50
	s_cbranch_scc1 .Lc_A0_flush7

.Lc_A0_skip7:
	s_branch .Lg_fin
.Lg_drainB:
	s_waitcnt vmcnt(7)
	s_cmp_eq_u32 s68, 16
	s_cbranch_scc1 .Lc_B0_skip8
	s_cmp_lg_u32 s68, s50
	s_cbranch_scc1 .Lc_B0_flush8

.Lc_B0_skip8:
	s_waitcnt vmcnt(6)
	s_cmp_eq_u32 s69, 16
	s_cbranch_scc1 .Lc_B0_skip9
	s_cmp_lg_u32 s69, s50
	s_cbranch_scc1 .Lc_B0_flush9

.Lc_B0_skip9:
	s_waitcnt vmcnt(5)
	s_cmp_eq_u32 s70, 16
	s_cbranch_scc1 .Lc_B0_skip10
	s_cmp_lg_u32 s70, s50
	s_cbranch_scc1 .Lc_B0_flush10

.Lc_B0_skip10:
	s_waitcnt vmcnt(4)
	s_cmp_eq_u32 s71, 16
	s_cbranch_scc1 .Lc_B0_skip11
	s_cmp_lg_u32 s71, s50
	s_cbranch_scc1 .Lc_B0_flush11

.Lc_B0_skip11:
	s_waitcnt vmcnt(3)
	s_cmp_eq_u32 s72, 16
	s_cbranch_scc1 .Lc_B0_skip12
	s_cmp_lg_u32 s72, s50
	s_cbranch_scc1 .Lc_B0_flush12

.Lc_B0_skip12:
	s_waitcnt vmcnt(2)
	s_cmp_eq_u32 s73, 16
	s_cbranch_scc1 .Lc_B0_skip13
	s_cmp_lg_u32 s73, s50
	s_cbranch_scc1 .Lc_B0_flush13

.Lc_B0_skip13:
	s_waitcnt vmcnt(1)
	s_cmp_eq_u32 s74, 16
	s_cbranch_scc1 .Lc_B0_skip14
	s_cmp_lg_u32 s74, s50
	s_cbranch_scc1 .Lc_B0_flush14

.Lc_B0_skip14:
	s_waitcnt vmcnt(0)
	s_cmp_eq_u32 s75, 16
	s_cbranch_scc1 .Lc_B0_skip15
	s_cmp_lg_u32 s75, s50
	s_cbranch_scc1 .Lc_B0_flush15

.Lc_B0_skip15:
.Lg_fin:
	s_mul_i32 s42, s50, 0x810
	v_add_u32_e32 v220, s42, v219
	ds_add_f64 v220, v[200:201] offset:32768
	ds_add_f64 v220, v[202:203] offset:33280
	ds_add_f64 v220, v[204:205] offset:33792
	ds_add_f64 v220, v[206:207] offset:34304
	s_branch .Lg_alldone

.Lc_B8_flush15:
	s_mul_i32 s42, s50, 0x810
	v_add_u32_e32 v220, s42, v219
	ds_add_f64 v220, v[200:201] offset:32768
	ds_add_f64 v220, v[202:203] offset:33280
	ds_add_f64 v220, v[204:205] offset:33792
	ds_add_f64 v220, v[206:207] offset:34304
	v_mov_b32_e32 v200, 0
	v_mov_b32_e32 v201, 0
	v_mov_b32_e32 v202, 0
	v_mov_b32_e32 v203, 0
	v_mov_b32_e32 v204, 0
	v_mov_b32_e32 v205, 0
	v_mov_b32_e32 v206, 0
	v_mov_b32_e32 v207, 0
	s_mov_b32 s50, s75
	s_branch .Lc_B8_cont15
.Lc_A0_flush0:
	s_mul_i32 s42, s50, 0x810
	v_add_u32_e32 v220, s42, v219
	ds_add_f64 v220, v[200:201] offset:32768
	ds_add_f64 v220, v[202:203] offset:33280
	ds_add_f64 v220, v[204:205] offset:33792
	ds_add_f64 v220, v[206:207] offset:34304
	v_mov_b32_e32 v200, 0
	v_mov_b32_e32 v201, 0
	v_mov_b32_e32 v202, 0
	v_mov_b32_e32 v203, 0
	v_mov_b32_e32 v204, 0
	v_mov_b32_e32 v205, 0
	v_mov_b32_e32 v206, 0
	v_mov_b32_e32 v207, 0
	s_mov_b32 s50, s60
	s_branch .Lc_A0_cont0

.Lg_alldone:
	s_waitcnt vmcnt(0)
	v_mul_f32_e32 v150, v62, v62
	v_mul_f32_e32 v151, v63, v63
	v_mul_f32_e32 v152, v64, v64
	v_mul_f32_e32 v153, v65, v65
	v_fmac_f32_e32 v150, v58, v58
	v_fmac_f32_e32 v151, v59, v59
	v_fmac_f32_e32 v152, v60, v60
	v_fmac_f32_e32 v153, v61, v61
	v_fmac_f32_e32 v150, v54, v54
	v_fmac_f32_e32 v151, v55, v55
	v_fmac_f32_e32 v152, v56, v56
	v_fmac_f32_e32 v153, v57, v57
	v_fmac_f32_e32 v150, v50, v50
	v_fmac_f32_e32 v151, v51, v51
	v_fmac_f32_e32 v152, v52, v52
	v_fmac_f32_e32 v153, v53, v53
	v_fmac_f32_e32 v150, v46, v46
	v_fmac_f32_e32 v151, v47, v47
	v_fmac_f32_e32 v152, v48, v48
	v_fmac_f32_e32 v153, v49, v49
	v_fmac_f32_e32 v150, v42, v42
	v_fmac_f32_e32 v151, v43, v43
	v_fmac_f32_e32 v152, v44, v44
	v_fmac_f32_e32 v153, v45, v45
	v_fmac_f32_e32 v150, v38, v38
	v_fmac_f32_e32 v151, v39, v39
	v_fmac_f32_e32 v152, v40, v40
	v_fmac_f32_e32 v153, v41, v41
	v_fmac_f32_e32 v150, v34, v34
	v_fmac_f32_e32 v151, v35, v35
	v_fmac_f32_e32 v152, v36, v36
	v_fmac_f32_e32 v153, v37, v37
	v_fmac_f32_e32 v150, v30, v30
	v_fmac_f32_e32 v151, v31, v31
	v_fmac_f32_e32 v152, v32, v32
	v_fmac_f32_e32 v153, v33, v33
	v_fmac_f32_e32 v150, v26, v26
	v_fmac_f32_e32 v151, v27, v27
	v_fmac_f32_e32 v152, v28, v28
	v_fmac_f32_e32 v153, v29, v29
	v_fmac_f32_e32 v150, v22, v22
	v_fmac_f32_e32 v151, v23, v23
	v_fmac_f32_e32 v152, v24, v24
	v_fmac_f32_e32 v153, v25, v25
	v_fmac_f32_e32 v150, v18, v18
	v_fmac_f32_e32 v151, v19, v19
	v_fmac_f32_e32 v152, v20, v20
	v_fmac_f32_e32 v153, v21, v21
	v_fmac_f32_e32 v150, v14, v14
	v_fmac_f32_e32 v151, v15, v15
	v_fmac_f32_e32 v152, v16, v16
	v_fmac_f32_e32 v153, v17, v17
	v_fmac_f32_e32 v150, v10, v10
	v_fmac_f32_e32 v151, v11, v11
	v_fmac_f32_e32 v152, v12, v12
	v_fmac_f32_e32 v153, v13, v13
	v_fmac_f32_e32 v150, v6, v6
	v_fmac_f32_e32 v151, v7, v7
	v_fmac_f32_e32 v152, v8, v8
	v_fmac_f32_e32 v153, v9, v9
	v_fmac_f32_e32 v150, v2, v2
	v_fmac_f32_e32 v151, v3, v3
	v_fmac_f32_e32 v152, v4, v4
	v_fmac_f32_e32 v153, v5, v5
	v_add_f32_e32 v150, v150, v151
	v_add_f32_e32 v152, v152, v153
	v_add_f32_e32 v150, v150, v152
	v_mbcnt_lo_u32_b32 v151, -1, 0
	v_mbcnt_hi_u32_b32 v151, -1, v151
	v_xor_b32_e32 v152, 16, v151
	v_lshlrev_b32_e32 v152, 2, v152
	ds_bpermute_b32 v152, v152, v150
	v_xor_b32_e32 v153, 32, v151
	v_lshlrev_b32_e32 v153, 2, v153
	s_waitcnt lgkmcnt(0)
	v_add_f32_e32 v150, v150, v152
	ds_bpermute_b32 v153, v153, v150
	v_add_u32_e32 v152, s24, v1
	v_lshlrev_b32_e32 v152, 2, v152
	v_add_u32_e32 v152, 0x11300, v152
	v_cmp_gt_u32_e32 vcc, 16, v1
	s_and_saveexec_b64 s[30:31], vcc
	s_waitcnt lgkmcnt(0)
	v_add_f32_e32 v150, v150, v153
	ds_write_b32 v152, v150
	s_mov_b64 exec, s[30:31]
	v_and_b32_e32 v138, 15, v0
	v_or_b32_e32 v134, s24, v138
	v_lshlrev_b32_e32 v135, 3, v1
	v_lshlrev_b32_e32 v139, 2, v1
	v_bfe_u32 v140, v0, 4, 2
	v_cmp_eq_u32_e64 s[2:3], 0, v1

amdhsa.kernels:
  - .agpr_count:     4
    .args:
      - .actual_access:  read_only
        .address_space:  global
        .offset:         0
        .size:           8
        .value_kind:     global_buffer
      - .actual_access:  read_only
        .address_space:  global
        .offset:         8
        .size:           8
        .value_kind:     global_buffer
      - .actual_access:  read_only
        .address_space:  global
        .offset:         16
        .size:           8
        .value_kind:     global_buffer
      - .actual_access:  write_only
        .address_space:  global
        .offset:         24
        .size:           8
        .value_kind:     global_buffer
      - .actual_access:  write_only
        .address_space:  global
        .offset:         32
        .size:           8
        .value_kind:     global_buffer
      - .actual_access:  write_only
        .address_space:  global
        .offset:         40
        .size:           8
        .value_kind:     global_buffer
      - .actual_access:  write_only
        .address_space:  global
        .offset:         48
        .size:           8
        .value_kind:     global_buffer
    .group_segment_fixed_size: 71936
    .kernarg_segment_align: 8
    .kernarg_segment_size: 56
    .language:       OpenCL C
    .language_version:
      - 2
      - 0
    .max_flat_workgroup_size: 256
    .name:           _Z7vq_mainPKfPKiS0_PfPhPdPi
    .private_segment_fixed_size: 0
    .sgpr_count:     108
    .sgpr_spill_count: 0
    .symbol:         _Z7vq_mainPKfPKiS0_PfPhPdPi.kd
    .uniform_work_group_size: 1
    .uses_dynamic_stack: false
    .vgpr_count:     228
    .vgpr_spill_count: 0
    .wavefront_size: 64
  - .agpr_count:     0
    .args:
      - .actual_access:  read_only
        .address_space:  global
        .offset:         0
        .size:           8
        .value_kind:     global_buffer
      - .actual_access:  read_only
        .address_space:  global
        .offset:         8
        .size:           8
        .value_kind:     global_buffer
      - .actual_access:  read_only
        .address_space:  global
        .offset:         16
        .size:           8
        .value_kind:     global_buffer
      - .actual_access:  write_only
        .address_space:  global
        .offset:         24
        .size:           8
        .value_kind:     global_buffer
    .group_segment_fixed_size: 352
    .kernarg_segment_align: 8
    .kernarg_segment_size: 32
    .language:       OpenCL C
    .language_version:
      - 2
      - 0
    .max_flat_workgroup_size: 1024
    .name:           _Z11vq_finalizePK15HIP_vector_typeIjLj4EEPKdPKiPf
    .private_segment_fixed_size: 0
    .sgpr_count:     30
    .sgpr_spill_count: 0
    .symbol:         _Z11vq_finalizePK15HIP_vector_typeIjLj4EEPKdPKiPf.kd
    .uniform_work_group_size: 1
    .uses_dynamic_stack: false
    .vgpr_count:     24
    .vgpr_spill_count: 0
    .wavefront_size: 64
